# P0: also the weight-transpose source loads marked non-temporal (f32 weights streamed once)
# speedup vs baseline: 1.0201x; 1.0082x over previous
; #define LAS __attribute__((address_space(3)))
; __device__ __forceinline__ void transpose_item(const float* W, int N, int k0, int n0, bf16_t* WT, int ldk, int dst_row0, LAS float* scr, int lane, const float* kgain) {
;     float v[32];
; #pragma unroll
;     for (int i = 0; i < 32; ++i) v[i] = W[(size_t)(k0 + 2 * i + (lane >> 5)) * N + n0 + (lane & 31)];
.LBB0_31:
	s_ashr_i32 s23, s22, 31
	s_lshl_b32 s24, s19, 6
	s_lshl_b64 s[26:27], s[22:23], 2
	v_add_u32_e32 v18, s24, v21
	s_add_u32 s26, s6, s26
	s_addc_u32 s27, s17, s27
	v_ashrrev_i32_e32 v2, 31, v18
	v_lshl_add_u64 v[0:1], s[26:27], 0, v[24:25]
	v_mul_lo_u32 v4, s4, v2
	v_mul_lo_u32 v5, s5, v18
	v_mad_u64_u32 v[2:3], s[26:27], s4, v18, 0
	v_add3_u32 v3, v3, v4, v5
	v_add_u32_e32 v4, 2, v18
	v_ashrrev_i32_e32 v5, 31, v4
	v_mul_lo_u32 v6, s4, v5
	v_mul_lo_u32 v7, s5, v4
	v_mad_u64_u32 v[4:5], s[26:27], s4, v4, 0
	v_add3_u32 v5, v5, v6, v7
	v_add_u32_e32 v6, 4, v18
	v_ashrrev_i32_e32 v7, 31, v6
	v_mul_lo_u32 v8, s4, v7
	v_mul_lo_u32 v9, s5, v6
	v_mad_u64_u32 v[6:7], s[26:27], s4, v6, 0
	v_add3_u32 v7, v7, v8, v9
	v_add_u32_e32 v8, 6, v18
	v_ashrrev_i32_e32 v9, 31, v8
	v_mul_lo_u32 v10, s4, v9
	v_mul_lo_u32 v11, s5, v8
	v_mad_u64_u32 v[8:9], s[26:27], s4, v8, 0
	v_add3_u32 v9, v9, v10, v11
	v_add_u32_e32 v10, 8, v18
	v_ashrrev_i32_e32 v11, 31, v10
	v_mul_lo_u32 v12, s4, v11
	v_mul_lo_u32 v13, s5, v10
	v_mad_u64_u32 v[10:11], s[26:27], s4, v10, 0
	v_add3_u32 v11, v11, v12, v13
	v_add_u32_e32 v12, 10, v18
	v_ashrrev_i32_e32 v13, 31, v12
	v_mul_lo_u32 v14, s4, v13
	v_mul_lo_u32 v15, s5, v12
	v_mad_u64_u32 v[12:13], s[26:27], s4, v12, 0
	v_add3_u32 v13, v13, v14, v15
	v_add_u32_e32 v14, 12, v18
	v_ashrrev_i32_e32 v15, 31, v14
	v_mul_lo_u32 v16, s4, v15
	v_mul_lo_u32 v17, s5, v14
	v_mad_u64_u32 v[14:15], s[26:27], s4, v14, 0
	v_add3_u32 v15, v15, v16, v17
	v_add_u32_e32 v16, 14, v18
	v_ashrrev_i32_e32 v17, 31, v16
	v_mul_lo_u32 v19, s4, v17
	v_mul_lo_u32 v29, s5, v16
	v_mad_u64_u32 v[16:17], s[26:27], s4, v16, 0
	v_lshl_add_u64 v[2:3], v[2:3], 2, v[0:1]
	v_add3_u32 v17, v17, v19, v29
	v_lshl_add_u64 v[4:5], v[4:5], 2, v[0:1]
	v_lshl_add_u64 v[6:7], v[6:7], 2, v[0:1]
	v_lshl_add_u64 v[8:9], v[8:9], 2, v[0:1]
	v_lshl_add_u64 v[10:11], v[10:11], 2, v[0:1]
	v_lshl_add_u64 v[12:13], v[12:13], 2, v[0:1]
	v_lshl_add_u64 v[14:15], v[14:15], 2, v[0:1]
	v_lshl_add_u64 v[16:17], v[16:17], 2, v[0:1]
	global_load_dword v19, v[2:3], off nt
	global_load_dword v29, v[4:5], off nt
	global_load_dword v30, v[6:7], off nt
	global_load_dword v31, v[8:9], off nt
	global_load_dword v32, v[10:11], off nt
	global_load_dword v33, v[12:13], off nt
	global_load_dword v34, v[14:15], off nt
	global_load_dword v35, v[16:17], off nt
	v_add_u32_e32 v2, 16, v18
	v_ashrrev_i32_e32 v3, 31, v2
	v_mul_lo_u32 v4, s4, v3
	v_mul_lo_u32 v5, s5, v2
	v_mad_u64_u32 v[2:3], s[26:27], s4, v2, 0
	v_add3_u32 v3, v3, v4, v5
	v_add_u32_e32 v4, 18, v18
	v_ashrrev_i32_e32 v5, 31, v4
	v_mul_lo_u32 v6, s4, v5
	v_mul_lo_u32 v7, s5, v4
	v_mad_u64_u32 v[4:5], s[26:27], s4, v4, 0
	v_add3_u32 v5, v5, v6, v7
	v_add_u32_e32 v6, 20, v18
	v_ashrrev_i32_e32 v7, 31, v6
	v_mul_lo_u32 v8, s4, v7
	v_mul_lo_u32 v9, s5, v6
	v_mad_u64_u32 v[6:7], s[26:27], s4, v6, 0
	v_add3_u32 v7, v7, v8, v9
	v_add_u32_e32 v8, 22, v18
	v_ashrrev_i32_e32 v9, 31, v8
	v_mul_lo_u32 v10, s4, v9
	v_mul_lo_u32 v11, s5, v8
	v_mad_u64_u32 v[8:9], s[26:27], s4, v8, 0
	v_add3_u32 v9, v9, v10, v11
	v_add_u32_e32 v10, 24, v18
	v_ashrrev_i32_e32 v11, 31, v10
	v_mul_lo_u32 v12, s4, v11
	v_mul_lo_u32 v13, s5, v10
	v_mad_u64_u32 v[10:11], s[26:27], s4, v10, 0
	v_add3_u32 v11, v11, v12, v13
	v_add_u32_e32 v12, 26, v18
	v_ashrrev_i32_e32 v13, 31, v12
	v_mul_lo_u32 v14, s4, v13
	v_mul_lo_u32 v15, s5, v12
	v_mad_u64_u32 v[12:13], s[26:27], s4, v12, 0
	v_add3_u32 v13, v13, v14, v15
	v_add_u32_e32 v14, 28, v18
	v_ashrrev_i32_e32 v15, 31, v14
	v_mul_lo_u32 v16, s4, v15
	v_mul_lo_u32 v17, s5, v14
	v_mad_u64_u32 v[14:15], s[26:27], s4, v14, 0
	v_add3_u32 v15, v15, v16, v17
	v_add_u32_e32 v16, 30, v18
	v_ashrrev_i32_e32 v17, 31, v16
	v_mul_lo_u32 v36, s4, v17
	v_mul_lo_u32 v37, s5, v16
	v_mad_u64_u32 v[16:17], s[26:27], s4, v16, 0
	v_lshl_add_u64 v[2:3], v[2:3], 2, v[0:1]
	v_add3_u32 v17, v17, v36, v37
	v_lshl_add_u64 v[4:5], v[4:5], 2, v[0:1]
	v_lshl_add_u64 v[6:7], v[6:7], 2, v[0:1]
	v_lshl_add_u64 v[8:9], v[8:9], 2, v[0:1]
	v_lshl_add_u64 v[10:11], v[10:11], 2, v[0:1]
	v_lshl_add_u64 v[12:13], v[12:13], 2, v[0:1]
	v_lshl_add_u64 v[14:15], v[14:15], 2, v[0:1]
	v_lshl_add_u64 v[16:17], v[16:17], 2, v[0:1]
	global_load_dword v36, v[2:3], off nt
	global_load_dword v37, v[4:5], off nt
	global_load_dword v38, v[6:7], off nt
	global_load_dword v39, v[8:9], off nt
	global_load_dword v40, v[10:11], off nt
	global_load_dword v41, v[12:13], off nt
	global_load_dword v42, v[14:15], off nt
	global_load_dword v43, v[16:17], off nt
	v_add_u32_e32 v2, 32, v18
	v_ashrrev_i32_e32 v3, 31, v2
	v_mul_lo_u32 v4, s4, v3
	v_mul_lo_u32 v5, s5, v2
	v_mad_u64_u32 v[2:3], s[26:27], s4, v2, 0
	v_add3_u32 v3, v3, v4, v5
	v_add_u32_e32 v4, 34, v18
	v_ashrrev_i32_e32 v5, 31, v4
	v_mul_lo_u32 v6, s4, v5
	v_mul_lo_u32 v7, s5, v4
	v_mad_u64_u32 v[4:5], s[26:27], s4, v4, 0
	v_add3_u32 v5, v5, v6, v7
	v_add_u32_e32 v6, 36, v18
	v_ashrrev_i32_e32 v7, 31, v6
	v_mul_lo_u32 v8, s4, v7
	v_mul_lo_u32 v9, s5, v6
	v_mad_u64_u32 v[6:7], s[26:27], s4, v6, 0
	v_add3_u32 v7, v7, v8, v9
	v_add_u32_e32 v8, 38, v18
	v_ashrrev_i32_e32 v9, 31, v8
	v_mul_lo_u32 v10, s4, v9
	v_mul_lo_u32 v11, s5, v8
	v_mad_u64_u32 v[8:9], s[26:27], s4, v8, 0
	v_add3_u32 v9, v9, v10, v11
	v_add_u32_e32 v10, 40, v18
	v_ashrrev_i32_e32 v11, 31, v10
	v_mul_lo_u32 v12, s4, v11
	v_mul_lo_u32 v13, s5, v10
	v_mad_u64_u32 v[10:11], s[26:27], s4, v10, 0
	v_add3_u32 v11, v11, v12, v13
	v_add_u32_e32 v12, 42, v18
	v_ashrrev_i32_e32 v13, 31, v12
	v_mul_lo_u32 v14, s4, v13
	v_mul_lo_u32 v15, s5, v12
	v_mad_u64_u32 v[12:13], s[26:27], s4, v12, 0
	v_add3_u32 v13, v13, v14, v15
	v_add_u32_e32 v14, 44, v18
	v_ashrrev_i32_e32 v15, 31, v14
; #define LAS __attribute__((address_space(3)))
; #define LDS_WAIT() asm volatile("s_waitcnt lgkmcnt(0)" ::: "memory")
; __device__ __forceinline__ unsigned cvt_pk_bf16(float lo, float hi) { unsigned r; asm volatile("v_cvt_pk_bf16_f32 %0, %1, %2" : "=v"(r) : "v"(lo), "v"(hi)); return r; }
; __device__ __forceinline__ void transpose_item(const float* W, int N, int k0, int n0, bf16_t* WT, int ldk, int dst_row0, LAS float* scr, int lane, const float* kgain) {
;     ...
;     for (int i = 0; i < 32; ++i) v[i] = W[(size_t)(k0 + 2 * i + (lane >> 5)) * N + n0 + (lane & 31)];
;     if (kgain) {
; #pragma unroll
;         for (int i = 0; i < 32; ++i) v[i] *= kgain[k0 + 2 * i + (lane >> 5)]; }
; #pragma unroll
;     for (int i = 0; i < 32; ++i) { const int kk = 2 * i + (lane >> 5); scr[kk * 32 + ((lane & 31) ^ ((kk >> 3) << 2))] = v[i]; }
;     LDS_WAIT(); asm volatile("" ::: "memory");
;     const int c = lane & 7;
; #pragma unroll
;     for (int j = 0; j < 4; ++j) { const int n = (lane >> 3) + 8 * j; const LAS float* s = scr + (8 * c) * 32 + (n ^ (c << 2));
;         u32x4 o; o.x = cvt_pk_bf16(s[0 * 32], s[1 * 32]); o.y = cvt_pk_bf16(s[2 * 32], s[3 * 32]); o.z = cvt_pk_bf16(s[4 * 32], s[5 * 32]); o.w = cvt_pk_bf16(s[6 * 32], s[7 * 32]);
;         *(u32x4*)(WT + (size_t)(dst_row0 + n) * ldk + k0 + 8 * c) = o; }
	v_mul_lo_u32 v16, s4, v15
	v_mul_lo_u32 v17, s5, v14
	v_mad_u64_u32 v[14:15], s[26:27], s4, v14, 0
	v_add3_u32 v15, v15, v16, v17
	v_add_u32_e32 v16, 46, v18
	v_ashrrev_i32_e32 v17, 31, v16
	v_mul_lo_u32 v44, s4, v17
	v_mul_lo_u32 v45, s5, v16
	v_mad_u64_u32 v[16:17], s[26:27], s4, v16, 0
	v_lshl_add_u64 v[2:3], v[2:3], 2, v[0:1]
	v_add3_u32 v17, v17, v44, v45
	v_lshl_add_u64 v[4:5], v[4:5], 2, v[0:1]
	v_lshl_add_u64 v[6:7], v[6:7], 2, v[0:1]
	v_lshl_add_u64 v[8:9], v[8:9], 2, v[0:1]
	v_lshl_add_u64 v[10:11], v[10:11], 2, v[0:1]
	v_lshl_add_u64 v[12:13], v[12:13], 2, v[0:1]
	v_lshl_add_u64 v[14:15], v[14:15], 2, v[0:1]
	v_lshl_add_u64 v[16:17], v[16:17], 2, v[0:1]
	global_load_dword v44, v[2:3], off nt
	global_load_dword v45, v[4:5], off nt
	global_load_dword v46, v[6:7], off nt
	global_load_dword v47, v[8:9], off nt
	global_load_dword v48, v[10:11], off nt
	global_load_dword v49, v[12:13], off nt
	global_load_dword v50, v[14:15], off nt
	global_load_dword v51, v[16:17], off nt
	v_add_u32_e32 v2, 48, v18
	v_ashrrev_i32_e32 v3, 31, v2
	v_mul_lo_u32 v4, s4, v3
	v_mul_lo_u32 v5, s5, v2
	v_mad_u64_u32 v[2:3], s[26:27], s4, v2, 0
	v_add3_u32 v3, v3, v4, v5
	v_add_u32_e32 v4, 50, v18
	v_ashrrev_i32_e32 v5, 31, v4
	v_mul_lo_u32 v6, s4, v5
	v_mul_lo_u32 v7, s5, v4
	v_mad_u64_u32 v[4:5], s[26:27], s4, v4, 0
	v_add3_u32 v5, v5, v6, v7
	v_add_u32_e32 v6, 52, v18
	v_ashrrev_i32_e32 v7, 31, v6
	v_mul_lo_u32 v8, s4, v7
	v_mul_lo_u32 v9, s5, v6
	v_mad_u64_u32 v[6:7], s[26:27], s4, v6, 0
	v_add3_u32 v7, v7, v8, v9
	v_add_u32_e32 v8, 54, v18
	v_ashrrev_i32_e32 v9, 31, v8
	v_mul_lo_u32 v10, s4, v9
	v_mul_lo_u32 v11, s5, v8
	v_mad_u64_u32 v[8:9], s[26:27], s4, v8, 0
	v_add3_u32 v9, v9, v10, v11
	v_add_u32_e32 v10, 56, v18
	v_ashrrev_i32_e32 v11, 31, v10
	v_mul_lo_u32 v12, s4, v11
	v_mul_lo_u32 v13, s5, v10
	v_mad_u64_u32 v[10:11], s[26:27], s4, v10, 0
	v_add3_u32 v11, v11, v12, v13
	v_add_u32_e32 v12, 58, v18
	v_ashrrev_i32_e32 v13, 31, v12
	v_mul_lo_u32 v14, s4, v13
	v_mul_lo_u32 v15, s5, v12
	v_mad_u64_u32 v[12:13], s[26:27], s4, v12, 0
	v_add3_u32 v13, v13, v14, v15
	v_add_u32_e32 v14, 60, v18
	v_ashrrev_i32_e32 v15, 31, v14
	v_mul_lo_u32 v16, s4, v15
	v_mul_lo_u32 v17, s5, v14
	v_mad_u64_u32 v[14:15], s[26:27], s4, v14, 0
	v_add3_u32 v15, v15, v16, v17
	v_add_u32_e32 v16, 62, v18
	v_ashrrev_i32_e32 v17, 31, v16
	v_mul_lo_u32 v18, s4, v17
	v_mul_lo_u32 v52, s5, v16
	v_mad_u64_u32 v[16:17], s[26:27], s4, v16, 0
	v_add3_u32 v17, v17, v18, v52
	v_lshl_add_u64 v[2:3], v[2:3], 2, v[0:1]
	v_lshl_add_u64 v[4:5], v[4:5], 2, v[0:1]
	v_lshl_add_u64 v[6:7], v[6:7], 2, v[0:1]
	v_lshl_add_u64 v[8:9], v[8:9], 2, v[0:1]
	v_lshl_add_u64 v[10:11], v[10:11], 2, v[0:1]
	v_lshl_add_u64 v[12:13], v[12:13], 2, v[0:1]
	v_lshl_add_u64 v[14:15], v[14:15], 2, v[0:1]
	v_lshl_add_u64 v[0:1], v[16:17], 2, v[0:1]
	global_load_dword v2, v[2:3], off nt
	s_nop 0
	global_load_dword v3, v[4:5], off nt
	s_nop 0
	global_load_dword v4, v[6:7], off nt
	global_load_dword v5, v[8:9], off nt
	s_nop 0
	global_load_dword v6, v[10:11], off nt
	global_load_dword v7, v[12:13], off nt
	global_load_dword v8, v[14:15], off nt
	s_nop 0
	global_load_dword v0, v[0:1], off nt
	s_waitcnt vmcnt(31)
	ds_write_b32 v23, v19
	s_waitcnt vmcnt(30)
	ds_write_b32 v98, v29
	s_waitcnt vmcnt(29)
	ds_write_b32 v99, v30
	s_waitcnt vmcnt(28)
	ds_write_b32 v100, v31
	s_waitcnt vmcnt(27)
	ds_write_b32 v101, v32
	s_waitcnt vmcnt(26)
	ds_write_b32 v102, v33
	s_waitcnt vmcnt(25)
	ds_write_b32 v103, v34
	s_waitcnt vmcnt(24)
	ds_write_b32 v104, v35
	s_waitcnt vmcnt(23)
	ds_write_b32 v105, v36
	s_waitcnt vmcnt(22)
	ds_write_b32 v106, v37
	s_waitcnt vmcnt(21)
	ds_write_b32 v107, v38
	s_waitcnt vmcnt(20)
	ds_write_b32 v108, v39
	s_waitcnt vmcnt(19)
	ds_write_b32 v109, v40
	s_waitcnt vmcnt(18)
	ds_write_b32 v110, v41
	s_waitcnt vmcnt(17)
	ds_write_b32 v111, v42
	s_waitcnt vmcnt(16)
	ds_write_b32 v112, v43
	s_waitcnt vmcnt(15)
	ds_write_b32 v113, v44
	s_waitcnt vmcnt(14)
	ds_write_b32 v114, v45
	s_waitcnt vmcnt(13)
	ds_write_b32 v117, v46
	s_waitcnt vmcnt(12)
	ds_write_b32 v121, v47
	s_waitcnt vmcnt(11)
	ds_write_b32 v125, v48
	s_waitcnt vmcnt(10)
	ds_write_b32 v129, v49
	s_waitcnt vmcnt(9)
	ds_write_b32 v133, v50
	s_waitcnt vmcnt(8)
	ds_write_b32 v137, v51
	s_waitcnt vmcnt(7)
	ds_write_b32 v141, v2
	s_waitcnt vmcnt(6)
	ds_write_b32 v145, v3
	s_waitcnt vmcnt(5)
	ds_write_b32 v149, v4
	s_waitcnt vmcnt(4)
	ds_write_b32 v151, v5
	s_waitcnt vmcnt(3)
	ds_write_b32 v153, v6
	s_waitcnt vmcnt(2)
	ds_write_b32 v155, v7
	s_waitcnt vmcnt(1)
	ds_write_b32 v157, v8
	s_waitcnt vmcnt(0)
	ds_write_b32 v159, v0
	s_waitcnt lgkmcnt(0)
	ds_read2_b32 v[0:1], v197 offset1:32
	s_waitcnt lgkmcnt(0)
	v_cvt_pk_bf16_f32 v0, v0, v1
	ds_read2_b32 v[2:3], v197 offset0:64 offset1:96
	s_ashr_i32 s25, s24, 31
	s_waitcnt lgkmcnt(0)
	v_cvt_pk_bf16_f32 v1, v2, v3
	ds_read2_b32 v[2:3], v197 offset0:128 offset1:160
	s_lshl_b64 s[24:25], s[24:25], 1
	s_waitcnt lgkmcnt(0)
	v_cvt_pk_bf16_f32 v2, v2, v3
	ds_read2_b32 v[4:5], v197 offset0:192 offset1:224
	s_add_u32 s24, s3, s24
	s_addc_u32 s25, s1, s25
	v_mov_b32_e32 v29, v25
	s_waitcnt lgkmcnt(0)
	v_cvt_pk_bf16_f32 v3, v4, v5
	v_ashrrev_i32_e32 v4, 31, v208
	v_lshl_add_u64 v[6:7], s[24:25], 0, v[28:29]
	v_mul_lo_u32 v10, s12, v4
	v_mul_lo_u32 v11, s13, v208
	v_mad_u64_u32 v[8:9], s[24:25], s12, v208, 0
	v_add3_u32 v9, v9, v10, v11
	v_lshl_add_u64 v[8:9], v[8:9], 1, v[6:7]
	ds_read2_b32 v[4:5], v198 offset1:32
	global_store_dwordx4 v[8:9], v[0:3], off
	v_mul_lo_u32 v11, s13, v207
	v_mad_u64_u32 v[8:9], s[24:25], s12, v207, 0
	s_waitcnt lgkmcnt(0)
	v_cvt_pk_bf16_f32 v0, v4, v5
	ds_read2_b32 v[2:3], v198 offset0:64 offset1:96
	s_waitcnt lgkmcnt(0)
; #define LAS __attribute__((address_space(3)))
; #define LDS_WAIT() asm volatile("s_waitcnt lgkmcnt(0)" ::: "memory")
; __device__ __forceinline__ unsigned cvt_pk_bf16(float lo, float hi) { unsigned r; asm volatile("v_cvt_pk_bf16_f32 %0, %1, %2" : "=v"(r) : "v"(lo), "v"(hi)); return r; }
; __device__ __forceinline__ void transpose_item(const float* W, int N, int k0, int n0, bf16_t* WT, int ldk, int dst_row0, LAS float* scr, int lane, const float* kgain) {
;     ...
;     for (int j = 0; j < 4; ++j) { const int n = (lane >> 3) + 8 * j; const LAS float* s = scr + (8 * c) * 32 + (n ^ (c << 2));
;         u32x4 o; o.x = cvt_pk_bf16(s[0 * 32], s[1 * 32]); o.y = cvt_pk_bf16(s[2 * 32], s[3 * 32]); o.z = cvt_pk_bf16(s[4 * 32], s[5 * 32]); o.w = cvt_pk_bf16(s[6 * 32], s[7 * 32]);
;         *(u32x4*)(WT + (size_t)(dst_row0 + n) * ldk + k0 + 8 * c) = o; }
;     LDS_WAIT(); asm volatile("" ::: "memory");
; }
; __device__ __forceinline__ void transpose_item_fp8(const float* W, int N, int k0, int n0, unsigned char* WT, int ldk, int dst_row0, LAS float* scr, int lane, const float* kgain) {
;     ...
;     for (int i = 0; i < 64; ++i) v[i] = W[(size_t)(k0 + 2 * i + (lane >> 5)) * N + n0 + (lane & 31)];
	v_cvt_pk_bf16_f32 v1, v2, v3
	ds_read2_b32 v[2:3], v198 offset0:128 offset1:160
	s_waitcnt lgkmcnt(0)
	v_cvt_pk_bf16_f32 v2, v2, v3
	ds_read2_b32 v[4:5], v198 offset0:192 offset1:224
	s_waitcnt lgkmcnt(0)
	v_cvt_pk_bf16_f32 v3, v4, v5
	v_ashrrev_i32_e32 v4, 31, v207
	v_mul_lo_u32 v10, s12, v4
	v_add3_u32 v9, v9, v10, v11
	v_lshl_add_u64 v[8:9], v[8:9], 1, v[6:7]
	ds_read2_b32 v[4:5], v199 offset1:32
	global_store_dwordx4 v[8:9], v[0:3], off
	v_mul_lo_u32 v11, s13, v206
	v_mad_u64_u32 v[8:9], s[24:25], s12, v206, 0
	s_waitcnt lgkmcnt(0)
	v_cvt_pk_bf16_f32 v0, v4, v5
	ds_read2_b32 v[2:3], v199 offset0:64 offset1:96
	s_waitcnt lgkmcnt(0)
	v_cvt_pk_bf16_f32 v1, v2, v3
	ds_read2_b32 v[2:3], v199 offset0:128 offset1:160
	s_waitcnt lgkmcnt(0)
	v_cvt_pk_bf16_f32 v2, v2, v3
	ds_read2_b32 v[4:5], v199 offset0:192 offset1:224
	s_waitcnt lgkmcnt(0)
	v_cvt_pk_bf16_f32 v3, v4, v5
	v_ashrrev_i32_e32 v4, 31, v206
	v_mul_lo_u32 v10, s12, v4
	v_add3_u32 v9, v9, v10, v11
	v_lshl_add_u64 v[8:9], v[8:9], 1, v[6:7]
	ds_read2_b32 v[4:5], v200 offset1:32
	global_store_dwordx4 v[8:9], v[0:3], off
	v_mul_lo_u32 v9, s13, v205
	s_waitcnt lgkmcnt(0)
	v_cvt_pk_bf16_f32 v0, v4, v5
	ds_read2_b32 v[2:3], v200 offset0:64 offset1:96
	s_waitcnt lgkmcnt(0)
	v_cvt_pk_bf16_f32 v1, v2, v3
	ds_read2_b32 v[2:3], v200 offset0:128 offset1:160
	s_waitcnt lgkmcnt(0)
	v_cvt_pk_bf16_f32 v2, v2, v3
	ds_read2_b32 v[4:5], v200 offset0:192 offset1:224
	s_waitcnt lgkmcnt(0)
	v_cvt_pk_bf16_f32 v3, v4, v5
	v_ashrrev_i32_e32 v4, 31, v205
	v_mul_lo_u32 v8, s12, v4
	v_mad_u64_u32 v[4:5], s[24:25], s12, v205, 0
	v_add3_u32 v5, v5, v8, v9
	v_lshl_add_u64 v[4:5], v[4:5], 1, v[6:7]
	global_store_dwordx4 v[4:5], v[0:3], off
	s_waitcnt lgkmcnt(0)
	s_cbranch_execnz .LBB0_13
.LBB0_32:
	s_lshl_b32 s24, s19, 7
	v_add_u32_e32 v29, s24, v21
	v_ashrrev_i32_e32 v0, 31, v29
	v_mul_lo_u32 v2, s4, v0
	v_mul_lo_u32 v3, s5, v29
	v_mad_u64_u32 v[0:1], s[26:27], s4, v29, 0
	v_add3_u32 v1, v1, v2, v3
	v_add_u32_e32 v2, 2, v29
	v_ashrrev_i32_e32 v3, 31, v2
	v_mul_lo_u32 v4, s4, v3
	v_mul_lo_u32 v5, s5, v2
	v_mad_u64_u32 v[2:3], s[26:27], s4, v2, 0
	v_add3_u32 v3, v3, v4, v5
	v_add_u32_e32 v4, 4, v29
	v_ashrrev_i32_e32 v5, 31, v4
	v_mul_lo_u32 v6, s4, v5
	v_mul_lo_u32 v7, s5, v4
	v_mad_u64_u32 v[4:5], s[26:27], s4, v4, 0
	v_add3_u32 v5, v5, v6, v7
	v_add_u32_e32 v6, 6, v29
	v_ashrrev_i32_e32 v7, 31, v6
	v_mul_lo_u32 v8, s4, v7
	v_mul_lo_u32 v9, s5, v6
	v_mad_u64_u32 v[6:7], s[26:27], s4, v6, 0
	v_add3_u32 v7, v7, v8, v9
	v_add_u32_e32 v8, 8, v29
	v_ashrrev_i32_e32 v9, 31, v8
	v_mul_lo_u32 v10, s4, v9
	v_mul_lo_u32 v11, s5, v8
	v_mad_u64_u32 v[8:9], s[26:27], s4, v8, 0
	v_add3_u32 v9, v9, v10, v11
	v_add_u32_e32 v10, 10, v29
	v_ashrrev_i32_e32 v11, 31, v10
	v_mul_lo_u32 v12, s4, v11
	v_mul_lo_u32 v13, s5, v10
	v_mad_u64_u32 v[10:11], s[26:27], s4, v10, 0
	v_add3_u32 v11, v11, v12, v13
	v_add_u32_e32 v12, 12, v29
	v_ashrrev_i32_e32 v13, 31, v12
	v_mul_lo_u32 v14, s4, v13
	v_mul_lo_u32 v15, s5, v12
	v_mad_u64_u32 v[12:13], s[26:27], s4, v12, 0
	v_add3_u32 v13, v13, v14, v15
	v_add_u32_e32 v14, 14, v29
	v_ashrrev_i32_e32 v15, 31, v14
	v_mul_lo_u32 v16, s4, v15
	v_mul_lo_u32 v17, s5, v14
	v_mad_u64_u32 v[14:15], s[26:27], s4, v14, 0
	v_add3_u32 v15, v15, v16, v17
	v_add_u32_e32 v16, 16, v29
	v_ashrrev_i32_e32 v17, 31, v16
	v_mul_lo_u32 v18, s4, v17
	v_mul_lo_u32 v19, s5, v16
	v_mad_u64_u32 v[16:17], s[26:27], s4, v16, 0
	v_add3_u32 v17, v17, v18, v19
	v_add_u32_e32 v18, 18, v29
	v_ashrrev_i32_e32 v19, 31, v18
	v_mul_lo_u32 v30, s4, v19
	v_mul_lo_u32 v31, s5, v18
	v_mad_u64_u32 v[18:19], s[26:27], s4, v18, 0
	v_add3_u32 v19, v19, v30, v31
	v_add_u32_e32 v30, 20, v29
	v_ashrrev_i32_e32 v31, 31, v30
	v_mul_lo_u32 v32, s4, v31
	v_mul_lo_u32 v33, s5, v30
	v_mad_u64_u32 v[30:31], s[26:27], s4, v30, 0
	v_add3_u32 v31, v31, v32, v33
	v_add_u32_e32 v32, 22, v29
	v_ashrrev_i32_e32 v33, 31, v32
	v_mul_lo_u32 v34, s4, v33
	v_mul_lo_u32 v35, s5, v32
	v_mad_u64_u32 v[32:33], s[26:27], s4, v32, 0
	v_add3_u32 v33, v33, v34, v35
	v_add_u32_e32 v34, 24, v29
	v_ashrrev_i32_e32 v35, 31, v34
	v_mul_lo_u32 v36, s4, v35
	v_mul_lo_u32 v37, s5, v34
	v_mad_u64_u32 v[34:35], s[26:27], s4, v34, 0
	v_add3_u32 v35, v35, v36, v37
	v_add_u32_e32 v36, 26, v29
	v_ashrrev_i32_e32 v37, 31, v36
	v_mul_lo_u32 v38, s4, v37
	v_mul_lo_u32 v39, s5, v36
	v_mad_u64_u32 v[36:37], s[26:27], s4, v36, 0
	v_add3_u32 v37, v37, v38, v39
	v_add_u32_e32 v38, 28, v29
	v_ashrrev_i32_e32 v39, 31, v38
	v_mul_lo_u32 v40, s4, v39
	v_mul_lo_u32 v41, s5, v38
	v_mad_u64_u32 v[38:39], s[26:27], s4, v38, 0
	v_add3_u32 v39, v39, v40, v41
	v_add_u32_e32 v40, 30, v29
	v_ashrrev_i32_e32 v41, 31, v40
	v_mul_lo_u32 v42, s4, v41
	v_mul_lo_u32 v43, s5, v40
	v_mad_u64_u32 v[40:41], s[26:27], s4, v40, 0
	v_add3_u32 v41, v41, v42, v43
	v_add_u32_e32 v42, 32, v29
	v_ashrrev_i32_e32 v43, 31, v42
	v_mul_lo_u32 v44, s4, v43
	v_mul_lo_u32 v45, s5, v42
	v_mad_u64_u32 v[42:43], s[26:27], s4, v42, 0
	v_add3_u32 v43, v43, v44, v45
	v_add_u32_e32 v44, 34, v29
	v_ashrrev_i32_e32 v45, 31, v44
	v_mul_lo_u32 v46, s4, v45
	v_mul_lo_u32 v47, s5, v44
	v_mad_u64_u32 v[44:45], s[26:27], s4, v44, 0
	v_add3_u32 v45, v45, v46, v47
	v_add_u32_e32 v46, 36, v29
	v_ashrrev_i32_e32 v47, 31, v46
	v_mul_lo_u32 v48, s4, v47
	v_mul_lo_u32 v49, s5, v46
	v_mad_u64_u32 v[46:47], s[26:27], s4, v46, 0
	v_add3_u32 v47, v47, v48, v49
	v_add_u32_e32 v48, 38, v29
	v_ashrrev_i32_e32 v49, 31, v48
	v_mul_lo_u32 v50, s4, v49
	v_mul_lo_u32 v51, s5, v48
	v_mad_u64_u32 v[48:49], s[26:27], s4, v48, 0
	v_add3_u32 v49, v49, v50, v51
	v_add_u32_e32 v50, 40, v29
	v_ashrrev_i32_e32 v51, 31, v50
	v_mul_lo_u32 v52, s4, v51
	v_mul_lo_u32 v53, s5, v50
; __device__ __forceinline__ void transpose_item_fp8(const float* W, int N, int k0, int n0, unsigned char* WT, int ldk, int dst_row0, LAS float* scr, int lane, const float* kgain) {
;     ...
;     for (int i = 0; i < 64; ++i) v[i] = W[(size_t)(k0 + 2 * i + (lane >> 5)) * N + n0 + (lane & 31)];
	v_mad_u64_u32 v[50:51], s[26:27], s4, v50, 0
	v_add3_u32 v51, v51, v52, v53
	v_add_u32_e32 v52, 42, v29
	v_ashrrev_i32_e32 v53, 31, v52
	v_mul_lo_u32 v54, s4, v53
	v_mul_lo_u32 v55, s5, v52
	v_mad_u64_u32 v[52:53], s[26:27], s4, v52, 0
	v_add3_u32 v53, v53, v54, v55
	v_add_u32_e32 v54, 44, v29
	v_ashrrev_i32_e32 v55, 31, v54
	v_mul_lo_u32 v56, s4, v55
	v_mul_lo_u32 v57, s5, v54
	v_mad_u64_u32 v[54:55], s[26:27], s4, v54, 0
	v_add3_u32 v55, v55, v56, v57
	v_add_u32_e32 v56, 46, v29
	v_ashrrev_i32_e32 v57, 31, v56
	v_mul_lo_u32 v58, s4, v57
	v_mul_lo_u32 v59, s5, v56
	v_mad_u64_u32 v[56:57], s[26:27], s4, v56, 0
	v_add3_u32 v57, v57, v58, v59
	v_add_u32_e32 v58, 48, v29
	v_ashrrev_i32_e32 v59, 31, v58
	v_mul_lo_u32 v60, s4, v59
	v_mul_lo_u32 v61, s5, v58
	v_mad_u64_u32 v[58:59], s[26:27], s4, v58, 0
	v_add3_u32 v59, v59, v60, v61
	v_add_u32_e32 v60, 50, v29
	v_ashrrev_i32_e32 v61, 31, v60
	v_mul_lo_u32 v62, s4, v61
	v_mul_lo_u32 v63, s5, v60
	v_mad_u64_u32 v[60:61], s[26:27], s4, v60, 0
	v_add3_u32 v61, v61, v62, v63
	v_add_u32_e32 v62, 52, v29
	v_ashrrev_i32_e32 v63, 31, v62
	v_mul_lo_u32 v64, s4, v63
	v_mul_lo_u32 v65, s5, v62
	v_mad_u64_u32 v[62:63], s[26:27], s4, v62, 0
	v_add3_u32 v63, v63, v64, v65
	v_add_u32_e32 v64, 54, v29
	v_ashrrev_i32_e32 v65, 31, v64
	v_mul_lo_u32 v66, s4, v65
	v_mul_lo_u32 v67, s5, v64
	v_mad_u64_u32 v[64:65], s[26:27], s4, v64, 0
	v_add3_u32 v65, v65, v66, v67
	v_add_u32_e32 v66, 56, v29
	v_ashrrev_i32_e32 v67, 31, v66
	v_mul_lo_u32 v68, s4, v67
	v_mul_lo_u32 v69, s5, v66
	v_mad_u64_u32 v[66:67], s[26:27], s4, v66, 0
	v_add3_u32 v67, v67, v68, v69
	v_add_u32_e32 v68, 58, v29
	v_ashrrev_i32_e32 v69, 31, v68
	v_mul_lo_u32 v70, s4, v69
	v_mul_lo_u32 v71, s5, v68
	v_mad_u64_u32 v[68:69], s[26:27], s4, v68, 0
	v_add3_u32 v69, v69, v70, v71
	v_add_u32_e32 v70, 60, v29
	v_ashrrev_i32_e32 v71, 31, v70
	v_mul_lo_u32 v72, s4, v71
	v_mul_lo_u32 v73, s5, v70
	v_mad_u64_u32 v[70:71], s[26:27], s4, v70, 0
	v_add3_u32 v71, v71, v72, v73
	v_add_u32_e32 v72, 62, v29
	v_ashrrev_i32_e32 v73, 31, v72
	v_mul_lo_u32 v74, s4, v73
	v_mul_lo_u32 v75, s5, v72
	v_mad_u64_u32 v[72:73], s[26:27], s4, v72, 0
	v_add3_u32 v73, v73, v74, v75
	v_add_u32_e32 v74, 64, v29
	v_ashrrev_i32_e32 v75, 31, v74
	v_mul_lo_u32 v76, s4, v75
	v_mul_lo_u32 v77, s5, v74
	v_mad_u64_u32 v[74:75], s[26:27], s4, v74, 0
	v_add3_u32 v75, v75, v76, v77
	v_add_u32_e32 v76, 0x42, v29
	v_ashrrev_i32_e32 v77, 31, v76
	v_mul_lo_u32 v78, s4, v77
	v_mul_lo_u32 v79, s5, v76
	v_mad_u64_u32 v[76:77], s[26:27], s4, v76, 0
	v_add3_u32 v77, v77, v78, v79
	v_add_u32_e32 v78, 0x44, v29
	v_ashrrev_i32_e32 v79, 31, v78
	v_mul_lo_u32 v80, s4, v79
	v_mul_lo_u32 v81, s5, v78
	v_mad_u64_u32 v[78:79], s[26:27], s4, v78, 0
	v_add3_u32 v79, v79, v80, v81
	v_add_u32_e32 v80, 0x46, v29
	v_ashrrev_i32_e32 v81, 31, v80
	v_mul_lo_u32 v82, s4, v81
	v_mul_lo_u32 v83, s5, v80
	v_mad_u64_u32 v[80:81], s[26:27], s4, v80, 0
	v_add3_u32 v81, v81, v82, v83
	v_add_u32_e32 v82, 0x48, v29
	v_ashrrev_i32_e32 v83, 31, v82
	v_mul_lo_u32 v84, s4, v83
	v_mul_lo_u32 v85, s5, v82
	v_mad_u64_u32 v[82:83], s[26:27], s4, v82, 0
	v_add3_u32 v83, v83, v84, v85
	v_add_u32_e32 v84, 0x4a, v29
	v_ashrrev_i32_e32 v85, 31, v84
	v_mul_lo_u32 v86, s4, v85
	v_mul_lo_u32 v87, s5, v84
	v_mad_u64_u32 v[84:85], s[26:27], s4, v84, 0
	v_add3_u32 v85, v85, v86, v87
	v_add_u32_e32 v86, 0x4c, v29
	v_ashrrev_i32_e32 v87, 31, v86
	v_mul_lo_u32 v88, s4, v87
	v_mul_lo_u32 v89, s5, v86
	v_mad_u64_u32 v[86:87], s[26:27], s4, v86, 0
	v_add3_u32 v87, v87, v88, v89
	v_add_u32_e32 v88, 0x4e, v29
	v_ashrrev_i32_e32 v89, 31, v88
	v_mul_lo_u32 v90, s4, v89
	v_mul_lo_u32 v91, s5, v88
	v_mad_u64_u32 v[88:89], s[26:27], s4, v88, 0
	v_add3_u32 v89, v89, v90, v91
	v_add_u32_e32 v90, 0x50, v29
	v_ashrrev_i32_e32 v91, 31, v90
	v_mul_lo_u32 v92, s4, v91
	v_mul_lo_u32 v93, s5, v90
	v_mad_u64_u32 v[90:91], s[26:27], s4, v90, 0
	v_add3_u32 v91, v91, v92, v93
	v_add_u32_e32 v92, 0x52, v29
	v_ashrrev_i32_e32 v93, 31, v92
	v_mul_lo_u32 v94, s4, v93
	v_mul_lo_u32 v95, s5, v92
	v_mad_u64_u32 v[92:93], s[26:27], s4, v92, 0
	v_add3_u32 v93, v93, v94, v95
	v_add_u32_e32 v94, 0x54, v29
	v_ashrrev_i32_e32 v95, 31, v94
	v_mul_lo_u32 v96, s4, v95
	v_mul_lo_u32 v97, s5, v94
	v_mad_u64_u32 v[94:95], s[26:27], s4, v94, 0
	v_add3_u32 v95, v95, v96, v97
	v_add_u32_e32 v96, 0x56, v29
	v_ashrrev_i32_e32 v97, 31, v96
	v_mul_lo_u32 v209, s4, v97
	v_mul_lo_u32 v210, s5, v96
	v_mad_u64_u32 v[96:97], s[26:27], s4, v96, 0
	v_add3_u32 v97, v97, v209, v210
	v_add_u32_e32 v209, 0x58, v29
	v_ashrrev_i32_e32 v210, 31, v209
	v_mul_lo_u32 v212, s4, v210
	v_mul_lo_u32 v213, s5, v209
	v_mad_u64_u32 v[210:211], s[26:27], s4, v209, 0
	v_add_u32_e32 v209, 0x5a, v29
	v_add3_u32 v211, v211, v212, v213
	v_ashrrev_i32_e32 v212, 31, v209
	v_mul_lo_u32 v214, s4, v212
	v_mul_lo_u32 v215, s5, v209
	v_mad_u64_u32 v[212:213], s[26:27], s4, v209, 0
	v_add_u32_e32 v209, 0x5c, v29
	v_add3_u32 v213, v213, v214, v215
	v_ashrrev_i32_e32 v214, 31, v209
	v_mul_lo_u32 v216, s4, v214
	v_mul_lo_u32 v217, s5, v209
	v_mad_u64_u32 v[214:215], s[26:27], s4, v209, 0
	v_add_u32_e32 v209, 0x5e, v29
	v_add3_u32 v215, v215, v216, v217
	v_ashrrev_i32_e32 v216, 31, v209
	v_mul_lo_u32 v218, s4, v216
	v_mul_lo_u32 v219, s5, v209
	v_mad_u64_u32 v[216:217], s[26:27], s4, v209, 0
	v_add_u32_e32 v209, 0x60, v29
	v_add3_u32 v217, v217, v218, v219
	v_ashrrev_i32_e32 v218, 31, v209
	v_mul_lo_u32 v220, s4, v218
	v_mul_lo_u32 v221, s5, v209
	v_mad_u64_u32 v[218:219], s[26:27], s4, v209, 0
	v_add_u32_e32 v209, 0x62, v29
	v_add3_u32 v219, v219, v220, v221
	v_ashrrev_i32_e32 v220, 31, v209
	v_mul_lo_u32 v222, s4, v220
	v_mul_lo_u32 v223, s5, v209
; __device__ __forceinline__ void transpose_item_fp8(const float* W, int N, int k0, int n0, unsigned char* WT, int ldk, int dst_row0, LAS float* scr, int lane, const float* kgain) {
;     ...
;     for (int i = 0; i < 64; ++i) v[i] = W[(size_t)(k0 + 2 * i + (lane >> 5)) * N + n0 + (lane & 31)];
;     ...
;     for (int q = 0; q < 4; ++q) g[q] = kgain ? *(const f32x4*)(kgain + k0 + 16 * c + 4 * q) : (f32x4){1.f, 1.f, 1.f, 1.f};
	v_mad_u64_u32 v[220:221], s[26:27], s4, v209, 0
	v_add_u32_e32 v209, 0x64, v29
	v_add3_u32 v221, v221, v222, v223
	v_ashrrev_i32_e32 v222, 31, v209
	v_mul_lo_u32 v224, s4, v222
	v_mul_lo_u32 v225, s5, v209
	v_mad_u64_u32 v[222:223], s[26:27], s4, v209, 0
	v_add_u32_e32 v209, 0x66, v29
	v_add3_u32 v223, v223, v224, v225
	v_ashrrev_i32_e32 v224, 31, v209
	v_mul_lo_u32 v226, s4, v224
	v_mul_lo_u32 v227, s5, v209
	v_mad_u64_u32 v[224:225], s[26:27], s4, v209, 0
	v_add_u32_e32 v209, 0x68, v29
	v_add3_u32 v225, v225, v226, v227
	v_ashrrev_i32_e32 v226, 31, v209
	v_mul_lo_u32 v228, s4, v226
	v_mul_lo_u32 v229, s5, v209
	v_mad_u64_u32 v[226:227], s[26:27], s4, v209, 0
	v_add_u32_e32 v209, 0x6a, v29
	v_add3_u32 v227, v227, v228, v229
	v_ashrrev_i32_e32 v228, 31, v209
	v_mul_lo_u32 v230, s4, v228
	v_mul_lo_u32 v231, s5, v209
	v_mad_u64_u32 v[228:229], s[26:27], s4, v209, 0
	v_add_u32_e32 v209, 0x6c, v29
	v_add3_u32 v229, v229, v230, v231
	v_ashrrev_i32_e32 v230, 31, v209
	v_mul_lo_u32 v232, s4, v230
	v_mul_lo_u32 v233, s5, v209
	v_mad_u64_u32 v[230:231], s[26:27], s4, v209, 0
	v_add_u32_e32 v209, 0x6e, v29
	v_add3_u32 v231, v231, v232, v233
	v_ashrrev_i32_e32 v232, 31, v209
	v_mul_lo_u32 v234, s4, v232
	v_mul_lo_u32 v235, s5, v209
	v_mad_u64_u32 v[232:233], s[26:27], s4, v209, 0
	v_add_u32_e32 v209, 0x70, v29
	v_add3_u32 v233, v233, v234, v235
	v_ashrrev_i32_e32 v234, 31, v209
	v_mul_lo_u32 v236, s4, v234
	v_mul_lo_u32 v237, s5, v209
	v_mad_u64_u32 v[234:235], s[26:27], s4, v209, 0
	v_add_u32_e32 v209, 0x72, v29
	v_add3_u32 v235, v235, v236, v237
	v_ashrrev_i32_e32 v236, 31, v209
	v_mul_lo_u32 v238, s4, v236
	v_mul_lo_u32 v239, s5, v209
	v_mad_u64_u32 v[236:237], s[26:27], s4, v209, 0
	v_add_u32_e32 v209, 0x74, v29
	v_add3_u32 v237, v237, v238, v239
	v_ashrrev_i32_e32 v238, 31, v209
	v_mul_lo_u32 v240, s4, v238
	v_mul_lo_u32 v241, s5, v209
	v_mad_u64_u32 v[238:239], s[26:27], s4, v209, 0
	v_add_u32_e32 v209, 0x76, v29
	v_add3_u32 v239, v239, v240, v241
	v_ashrrev_i32_e32 v240, 31, v209
	v_mul_lo_u32 v242, s4, v240
	v_mul_lo_u32 v243, s5, v209
	v_mad_u64_u32 v[240:241], s[26:27], s4, v209, 0
	v_add_u32_e32 v209, 0x78, v29
	v_add3_u32 v241, v241, v242, v243
	v_ashrrev_i32_e32 v242, 31, v209
	v_mul_lo_u32 v244, s4, v242
	v_mul_lo_u32 v245, s5, v209
	v_mad_u64_u32 v[242:243], s[26:27], s4, v209, 0
	v_add_u32_e32 v209, 0x7a, v29
	v_add3_u32 v243, v243, v244, v245
	v_ashrrev_i32_e32 v244, 31, v209
	v_mul_lo_u32 v246, s4, v244
	v_mul_lo_u32 v247, s5, v209
	v_mad_u64_u32 v[244:245], s[26:27], s4, v209, 0
	v_add_u32_e32 v209, 0x7c, v29
	v_add3_u32 v245, v245, v246, v247
	v_ashrrev_i32_e32 v246, 31, v209
	v_add_u32_e32 v29, 0x7e, v29
	v_mul_lo_u32 v248, s4, v246
	v_mul_lo_u32 v249, s5, v209
	v_mad_u64_u32 v[246:247], s[26:27], s4, v209, 0
	v_ashrrev_i32_e32 v209, 31, v29
	v_add3_u32 v247, v247, v248, v249
	v_mul_lo_u32 v209, s4, v209
	v_mul_lo_u32 v250, s5, v29
	v_mad_u64_u32 v[248:249], s[4:5], s4, v29, 0
	s_and_b64 s[4:5], s[14:15], exec
	s_cselect_b32 s14, s10, 0
	s_cselect_b32 s15, s11, 0
	s_and_b64 s[4:5], s[20:21], exec
	s_cselect_b32 s5, s9, s15
	s_cselect_b32 s4, s8, s14
	s_ashr_i32 s23, s22, 31
	s_lshl_b64 s[14:15], s[22:23], 2
	s_add_u32 s14, s6, s14
	s_addc_u32 s15, s17, s15
	v_add3_u32 v249, v249, v209, v250
	v_lshl_add_u64 v[250:251], s[14:15], 0, v[24:25]
	v_lshl_add_u64 v[0:1], v[0:1], 2, v[250:251]
	v_lshl_add_u64 v[2:3], v[2:3], 2, v[250:251]
	global_load_dword v24, v[0:1], off nt
	global_load_dword v29, v[2:3], off nt
	v_lshl_add_u64 v[4:5], v[4:5], 2, v[250:251]
	v_lshl_add_u64 v[6:7], v[6:7], 2, v[250:251]
	global_load_dword v209, v[4:5], off nt
	v_lshl_add_u64 v[8:9], v[8:9], 2, v[250:251]
	v_lshl_add_u64 v[0:1], v[218:219], 2, v[250:251]
	global_load_dword v218, v[6:7], off nt
	global_load_dword v219, v[8:9], off nt
	v_lshl_add_u64 v[10:11], v[10:11], 2, v[250:251]
	v_lshl_add_u64 v[12:13], v[12:13], 2, v[250:251]
	v_lshl_add_u64 v[2:3], v[220:221], 2, v[250:251]
	global_load_dword v220, v[10:11], off nt
	global_load_dword v221, v[12:13], off nt
	v_lshl_add_u64 v[14:15], v[14:15], 2, v[250:251]
	v_lshl_add_u64 v[16:17], v[16:17], 2, v[250:251]
	v_lshl_add_u64 v[4:5], v[222:223], 2, v[250:251]
	global_load_dword v222, v[14:15], off nt
	global_load_dword v223, v[16:17], off nt
	v_lshl_add_u64 v[18:19], v[18:19], 2, v[250:251]
	v_lshl_add_u64 v[30:31], v[30:31], 2, v[250:251]
	v_lshl_add_u64 v[6:7], v[224:225], 2, v[250:251]
	global_load_dword v224, v[18:19], off nt
	global_load_dword v225, v[30:31], off nt
	v_lshl_add_u64 v[32:33], v[32:33], 2, v[250:251]
	v_lshl_add_u64 v[34:35], v[34:35], 2, v[250:251]
	v_lshl_add_u64 v[8:9], v[226:227], 2, v[250:251]
	global_load_dword v226, v[32:33], off nt
	global_load_dword v227, v[34:35], off nt
	v_lshl_add_u64 v[36:37], v[36:37], 2, v[250:251]
	v_lshl_add_u64 v[38:39], v[38:39], 2, v[250:251]
	v_lshl_add_u64 v[10:11], v[228:229], 2, v[250:251]
	global_load_dword v228, v[36:37], off nt
	global_load_dword v229, v[38:39], off nt
	v_lshl_add_u64 v[40:41], v[40:41], 2, v[250:251]
	v_lshl_add_u64 v[12:13], v[230:231], 2, v[250:251]
	global_load_dword v230, v[40:41], off nt
	v_lshl_add_u64 v[42:43], v[42:43], 2, v[250:251]
	v_lshl_add_u64 v[44:45], v[44:45], 2, v[250:251]
	v_lshl_add_u64 v[46:47], v[46:47], 2, v[250:251]
	v_lshl_add_u64 v[48:49], v[48:49], 2, v[250:251]
	v_lshl_add_u64 v[50:51], v[50:51], 2, v[250:251]
	v_lshl_add_u64 v[52:53], v[52:53], 2, v[250:251]
	v_lshl_add_u64 v[54:55], v[54:55], 2, v[250:251]
	v_lshl_add_u64 v[56:57], v[56:57], 2, v[250:251]
	v_lshl_add_u64 v[58:59], v[58:59], 2, v[250:251]
	v_lshl_add_u64 v[60:61], v[60:61], 2, v[250:251]
	v_lshl_add_u64 v[62:63], v[62:63], 2, v[250:251]
; __device__ __forceinline__ void transpose_item_fp8(const float* W, int N, int k0, int n0, unsigned char* WT, int ldk, int dst_row0, LAS float* scr, int lane, const float* kgain) {
;     ...
;     for (int i = 0; i < 64; ++i) v[i] = W[(size_t)(k0 + 2 * i + (lane >> 5)) * N + n0 + (lane & 31)];
; #pragma unroll
;     for (int i = 0; i < 64; ++i) { const int kk = 2 * i + (lane >> 5); scr[kk * 32 + ((lane & 31) ^ ((kk >> 4) << 2))] = v[i] * W8_SCALE; }
	v_lshl_add_u64 v[64:65], v[64:65], 2, v[250:251]
	v_lshl_add_u64 v[66:67], v[66:67], 2, v[250:251]
	v_lshl_add_u64 v[68:69], v[68:69], 2, v[250:251]
	v_lshl_add_u64 v[70:71], v[70:71], 2, v[250:251]
	v_lshl_add_u64 v[72:73], v[72:73], 2, v[250:251]
	v_lshl_add_u64 v[14:15], v[232:233], 2, v[250:251]
	v_lshl_add_u64 v[74:75], v[74:75], 2, v[250:251]
	v_lshl_add_u64 v[76:77], v[76:77], 2, v[250:251]
	v_lshl_add_u64 v[78:79], v[78:79], 2, v[250:251]
	v_lshl_add_u64 v[80:81], v[80:81], 2, v[250:251]
	v_lshl_add_u64 v[82:83], v[82:83], 2, v[250:251]
	v_lshl_add_u64 v[84:85], v[84:85], 2, v[250:251]
	v_lshl_add_u64 v[86:87], v[86:87], 2, v[250:251]
	v_lshl_add_u64 v[88:89], v[88:89], 2, v[250:251]
	v_lshl_add_u64 v[90:91], v[90:91], 2, v[250:251]
	v_lshl_add_u64 v[92:93], v[92:93], 2, v[250:251]
	v_lshl_add_u64 v[94:95], v[94:95], 2, v[250:251]
	v_lshl_add_u64 v[96:97], v[96:97], 2, v[250:251]
	v_lshl_add_u64 v[210:211], v[210:211], 2, v[250:251]
	v_lshl_add_u64 v[212:213], v[212:213], 2, v[250:251]
	v_lshl_add_u64 v[214:215], v[214:215], 2, v[250:251]
	v_lshl_add_u64 v[216:217], v[216:217], 2, v[250:251]
	v_lshl_add_u64 v[16:17], v[234:235], 2, v[250:251]
	v_lshl_add_u64 v[18:19], v[236:237], 2, v[250:251]
	v_lshl_add_u64 v[30:31], v[238:239], 2, v[250:251]
	v_lshl_add_u64 v[32:33], v[240:241], 2, v[250:251]
	v_lshl_add_u64 v[34:35], v[242:243], 2, v[250:251]
	v_lshl_add_u64 v[36:37], v[244:245], 2, v[250:251]
	v_lshl_add_u64 v[38:39], v[246:247], 2, v[250:251]
	v_lshl_add_u64 v[40:41], v[248:249], 2, v[250:251]
	global_load_dword v42, v[42:43], off nt
	s_nop 0
	global_load_dword v43, v[44:45], off nt
	s_nop 0
	global_load_dword v44, v[46:47], off nt
	global_load_dword v45, v[48:49], off nt
	s_nop 0
	global_load_dword v46, v[50:51], off nt
	global_load_dword v47, v[52:53], off nt
	global_load_dword v48, v[54:55], off nt
	global_load_dword v49, v[56:57], off nt
	s_nop 0
	global_load_dword v50, v[58:59], off nt
	global_load_dword v51, v[60:61], off nt
	global_load_dword v52, v[62:63], off nt
	global_load_dword v53, v[64:65], off nt
	global_load_dword v54, v[66:67], off nt
	global_load_dword v55, v[68:69], off nt
	global_load_dword v56, v[70:71], off nt
	global_load_dword v57, v[72:73], off nt
	global_load_dword v58, v[74:75], off nt
	global_load_dword v59, v[76:77], off nt
	global_load_dword v60, v[78:79], off nt
	global_load_dword v61, v[80:81], off nt
	global_load_dword v62, v[82:83], off nt
	global_load_dword v63, v[84:85], off nt
	global_load_dword v64, v[86:87], off nt
	global_load_dword v65, v[88:89], off nt
	global_load_dword v66, v[90:91], off nt
	global_load_dword v67, v[92:93], off nt
	global_load_dword v68, v[94:95], off nt
	global_load_dword v69, v[96:97], off nt
	global_load_dword v70, v[210:211], off nt
	global_load_dword v71, v[212:213], off nt
	global_load_dword v72, v[214:215], off nt
	global_load_dword v73, v[216:217], off nt
	s_nop 0
	global_load_dword v0, v[0:1], off nt
	s_nop 0
	global_load_dword v1, v[2:3], off nt
	s_nop 0
	global_load_dword v2, v[4:5], off nt
	global_load_dword v3, v[6:7], off nt
	s_nop 0
	global_load_dword v4, v[8:9], off nt
	global_load_dword v5, v[10:11], off nt
	global_load_dword v6, v[12:13], off nt
	global_load_dword v7, v[14:15], off nt
	s_nop 0
	global_load_dword v8, v[16:17], off nt
	global_load_dword v9, v[18:19], off nt
	global_load_dword v10, v[30:31], off nt
	global_load_dword v11, v[32:33], off nt
	global_load_dword v12, v[34:35], off nt
	global_load_dword v13, v[36:37], off nt
	global_load_dword v14, v[38:39], off nt
	global_load_dword v15, v[40:41], off nt
	s_cmp_lg_u64 s[4:5], 0
	s_waitcnt vmcnt(62)
	v_mul_f32_e32 v16, 0x42800000, v24
	ds_write_b32 v115, v16
	v_mul_f32_e32 v16, 0x42800000, v29
	ds_write_b32 v116, v16
	s_waitcnt vmcnt(61)
	v_mul_f32_e32 v16, 0x42800000, v209
	ds_write_b32 v118, v16
	s_cselect_b64 s[14:15], -1, 0
	s_waitcnt vmcnt(60)
	v_mul_f32_e32 v16, 0x42800000, v218
	ds_write_b32 v119, v16
	s_waitcnt vmcnt(59)
	v_mul_f32_e32 v16, 0x42800000, v219
	ds_write_b32 v120, v16
	s_ashr_i32 s25, s24, 31
	s_waitcnt vmcnt(58)
	v_mul_f32_e32 v16, 0x42800000, v220
	ds_write_b32 v122, v16
	s_waitcnt vmcnt(57)
	v_mul_f32_e32 v16, 0x42800000, v221
	ds_write_b32 v123, v16
	s_lshl_b64 s[20:21], s[24:25], 2
	s_waitcnt vmcnt(56)
	v_mul_f32_e32 v16, 0x42800000, v222
	ds_write_b32 v124, v16
	s_waitcnt vmcnt(55)
	v_mul_f32_e32 v16, 0x42800000, v223
	ds_write_b32 v126, v16
	s_add_u32 s20, s4, s20
	s_waitcnt vmcnt(54)
	v_mul_f32_e32 v16, 0x42800000, v224
	ds_write_b32 v127, v16
	s_waitcnt vmcnt(53)
	v_mul_f32_e32 v16, 0x42800000, v225
	ds_write_b32 v128, v16
	s_addc_u32 s21, s5, s21
	s_waitcnt vmcnt(52)
; #define LDS_WAIT() asm volatile("s_waitcnt lgkmcnt(0)" ::: "memory")
; __device__ __forceinline__ void transpose_item_fp8(const float* W, int N, int k0, int n0, unsigned char* WT, int ldk, int dst_row0, LAS float* scr, int lane, const float* kgain) {
;     ...
;     for (int i = 0; i < 64; ++i) { const int kk = 2 * i + (lane >> 5); scr[kk * 32 + ((lane & 31) ^ ((kk >> 4) << 2))] = v[i] * W8_SCALE; }
;     LDS_WAIT(); asm volatile("" ::: "memory");
;     const int c = lane & 7;
;     f32x4 g[4];
; #pragma unroll
;     for (int q = 0; q < 4; ++q) g[q] = kgain ? *(const f32x4*)(kgain + k0 + 16 * c + 4 * q) : (f32x4){1.f, 1.f, 1.f, 1.f};
	v_mul_f32_e32 v16, 0x42800000, v226
	ds_write_b32 v130, v16
	s_waitcnt vmcnt(51)
	v_mul_f32_e32 v16, 0x42800000, v227
	ds_write_b32 v131, v16
	v_lshlrev_b32_e32 v24, 2, v26
	s_waitcnt vmcnt(50)
	v_mul_f32_e32 v16, 0x42800000, v228
	ds_write_b32 v132, v16
	s_waitcnt vmcnt(49)
	v_mul_f32_e32 v16, 0x42800000, v229
	ds_write_b32 v134, v16
	s_waitcnt vmcnt(48)
	v_mul_f32_e32 v16, 0x42800000, v230
	ds_write_b32 v135, v16
	s_waitcnt vmcnt(47)
	v_mul_f32_e32 v16, 0x42800000, v42
	ds_write_b32 v136, v16
	s_waitcnt vmcnt(46)
	v_mul_f32_e32 v16, 0x42800000, v43
	ds_write_b32 v138, v16
	s_waitcnt vmcnt(45)
	v_mul_f32_e32 v16, 0x42800000, v44
	ds_write_b32 v139, v16
	s_waitcnt vmcnt(44)
	v_mul_f32_e32 v16, 0x42800000, v45
	ds_write_b32 v140, v16
	s_waitcnt vmcnt(43)
	v_mul_f32_e32 v16, 0x42800000, v46
	ds_write_b32 v142, v16
	s_waitcnt vmcnt(42)
	v_mul_f32_e32 v16, 0x42800000, v47
	ds_write_b32 v143, v16
	s_waitcnt vmcnt(41)
	v_mul_f32_e32 v16, 0x42800000, v48
	ds_write_b32 v144, v16
	s_waitcnt vmcnt(40)
	v_mul_f32_e32 v16, 0x42800000, v49
	ds_write_b32 v146, v16
	s_waitcnt vmcnt(39)
	v_mul_f32_e32 v16, 0x42800000, v50
	ds_write_b32 v147, v16
	s_waitcnt vmcnt(38)
	v_mul_f32_e32 v16, 0x42800000, v51
	ds_write_b32 v148, v16
	s_waitcnt vmcnt(37)
	v_mul_f32_e32 v16, 0x42800000, v52
	ds_write_b32 v150, v16
	s_waitcnt vmcnt(36)
	v_mul_f32_e32 v16, 0x42800000, v53
	ds_write_b32 v152, v16
	s_waitcnt vmcnt(35)
	v_mul_f32_e32 v16, 0x42800000, v54
	ds_write_b32 v154, v16
	s_waitcnt vmcnt(34)
	v_mul_f32_e32 v16, 0x42800000, v55
	ds_write_b32 v156, v16
	s_waitcnt vmcnt(33)
	v_mul_f32_e32 v16, 0x42800000, v56
	ds_write_b32 v158, v16
	s_waitcnt vmcnt(32)
	v_mul_f32_e32 v16, 0x42800000, v57
	ds_write_b32 v160, v16
	s_waitcnt vmcnt(31)
	v_mul_f32_e32 v16, 0x42800000, v58
	ds_write_b32 v161, v16
	s_waitcnt vmcnt(30)
	v_mul_f32_e32 v16, 0x42800000, v59
	ds_write_b32 v162, v16
	s_waitcnt vmcnt(29)
	v_mul_f32_e32 v16, 0x42800000, v60
	ds_write_b32 v163, v16
	s_waitcnt vmcnt(28)
	v_mul_f32_e32 v16, 0x42800000, v61
	ds_write_b32 v164, v16
	s_waitcnt vmcnt(27)
	v_mul_f32_e32 v16, 0x42800000, v62
	ds_write_b32 v165, v16
	s_waitcnt vmcnt(26)
	v_mul_f32_e32 v16, 0x42800000, v63
	ds_write_b32 v166, v16
	s_waitcnt vmcnt(25)
	v_mul_f32_e32 v16, 0x42800000, v64
	ds_write_b32 v167, v16
	s_waitcnt vmcnt(24)
	v_mul_f32_e32 v16, 0x42800000, v65
	ds_write_b32 v168, v16
	s_waitcnt vmcnt(23)
	v_mul_f32_e32 v16, 0x42800000, v66
	ds_write_b32 v169, v16
	s_waitcnt vmcnt(22)
	v_mul_f32_e32 v16, 0x42800000, v67
	ds_write_b32 v170, v16
	s_waitcnt vmcnt(21)
	v_mul_f32_e32 v16, 0x42800000, v68
	ds_write_b32 v171, v16
	s_waitcnt vmcnt(20)
	v_mul_f32_e32 v16, 0x42800000, v69
	ds_write_b32 v172, v16
	s_waitcnt vmcnt(19)
	v_mul_f32_e32 v16, 0x42800000, v70
	ds_write_b32 v173, v16
	s_waitcnt vmcnt(18)
	v_mul_f32_e32 v16, 0x42800000, v71
	ds_write_b32 v174, v16
	s_waitcnt vmcnt(17)
	v_mul_f32_e32 v16, 0x42800000, v72
	ds_write_b32 v175, v16
	s_waitcnt vmcnt(16)
	v_mul_f32_e32 v16, 0x42800000, v73
	s_waitcnt vmcnt(15)
	v_mul_f32_e32 v0, 0x42800000, v0
	ds_write_b32 v176, v16
	ds_write_b32 v177, v0
	s_waitcnt vmcnt(14)
	v_mul_f32_e32 v0, 0x42800000, v1
	ds_write_b32 v178, v0
	s_waitcnt vmcnt(13)
	v_mul_f32_e32 v0, 0x42800000, v2
	ds_write_b32 v179, v0
	s_waitcnt vmcnt(12)
	v_mul_f32_e32 v0, 0x42800000, v3
	ds_write_b32 v180, v0
	s_waitcnt vmcnt(11)
	v_mul_f32_e32 v0, 0x42800000, v4
	ds_write_b32 v181, v0
	s_waitcnt vmcnt(10)
	v_mul_f32_e32 v0, 0x42800000, v5
	ds_write_b32 v182, v0
	s_waitcnt vmcnt(9)
	v_mul_f32_e32 v0, 0x42800000, v6
	ds_write_b32 v183, v0
	s_waitcnt vmcnt(8)
	v_mul_f32_e32 v0, 0x42800000, v7
	ds_write_b32 v184, v0
	s_waitcnt vmcnt(7)
	v_mul_f32_e32 v0, 0x42800000, v8
	ds_write_b32 v185, v0
	s_waitcnt vmcnt(6)
	v_mul_f32_e32 v0, 0x42800000, v9
	ds_write_b32 v186, v0
	s_waitcnt vmcnt(5)
	v_mul_f32_e32 v0, 0x42800000, v10
	ds_write_b32 v187, v0
	s_waitcnt vmcnt(4)
	v_mul_f32_e32 v0, 0x42800000, v11
	ds_write_b32 v188, v0
	s_waitcnt vmcnt(3)
	v_mul_f32_e32 v0, 0x42800000, v12
	ds_write_b32 v189, v0
	s_waitcnt vmcnt(2)
	v_mul_f32_e32 v0, 0x42800000, v13
	ds_write_b32 v190, v0
	s_waitcnt vmcnt(1)
	v_mul_f32_e32 v0, 0x42800000, v14
	ds_write_b32 v191, v0
	s_waitcnt vmcnt(0)
	v_mul_f32_e32 v0, 0x42800000, v15
	ds_write_b32 v192, v0
	s_waitcnt lgkmcnt(0)
	s_cmp_eq_u64 s[4:5], 0
	v_lshl_add_u64 v[16:17], s[20:21], 0, v[24:25]
	v_mov_b32_e32 v0, 1.0
	v_mov_b32_e32 v4, 1.0
	v_mov_b32_e32 v5, 1.0
	v_mov_b32_e32 v6, 1.0
	v_mov_b32_e32 v7, 1.0
	s_cbranch_scc1 .LBB0_34
	global_load_dwordx4 v[4:7], v[16:17], off

; __global__ void __launch_bounds__(512, 2) fwd_kernel(Params p) {
;     ...
;         for (int i = GT(); i < NE * DM; i += NGT) { const int e = i / DM, k = i % DM; WrT[i] = p.in[I_GFFN][k] * p.in[I_WR][(size_t)k * NE + e]; }
.LBB0_43:
	v_ashrrev_i32_e32 v1, 31, v0
	v_lshrrev_b32_e32 v2, 21, v1
	v_add_u32_e32 v2, v0, v2
	v_ashrrev_i32_e32 v2, 11, v2
	v_mul_i32_i24_e32 v3, 0x800, v2
	v_sub_u32_e32 v4, v0, v3
	v_ashrrev_i32_e32 v5, 31, v4
	s_waitcnt lgkmcnt(0)
	v_lshl_add_u64 v[6:7], v[4:5], 2, s[4:5]
	v_lshlrev_b64 v[4:5], 7, v[4:5]
	v_ashrrev_i32_e32 v3, 31, v2
	v_lshl_add_u64 v[4:5], s[6:7], 0, v[4:5]
	v_lshl_add_u64 v[2:3], v[2:3], 2, v[4:5]
	global_load_dword v6, v[6:7], off nt
	s_nop 0
	global_load_dword v4, v[2:3], off nt
	v_lshl_add_u64 v[2:3], v[0:1], 2, s[30:31]
	v_add_u32_e32 v0, s83, v0
	v_cmp_lt_i32_e32 vcc, s0, v0
	s_or_b64 s[10:11], vcc, s[10:11]
	s_waitcnt vmcnt(0)
	v_mul_f32_e32 v1, v6, v4
	global_store_dword v[2:3], v1, off
	s_andn2_b64 exec, exec, s[10:11]
	s_cbranch_execnz .LBB0_43
